# speedup vs baseline: 1.0280x; 1.0000x over previous
_Z11attn_kernelPKDF16_S0_PDF16_P15HIP_vector_typeIfLj2EE:
	s_lshl_b32 s40, s3, 4
	s_add_u32 s40, s40, s2
	s_lshl_b32 s41, s4, 6
	s_add_u32 s40, s40, s41
	s_and_b32 s41, s40, 7
	s_lshr_b32 s40, s40, 3
	s_and_b32 s2, s41, 3
	s_lshl_b32 s2, s2, 2
	s_and_b32 s3, s40, 3
	s_or_b32 s2, s2, s3
	s_lshr_b32 s3, s40, 2
	s_and_b32 s3, s3, 3
	s_lshr_b32 s4, s41, 2
	s_lshl_b32 s4, s4, 1
	s_lshr_b32 s40, s40, 4
	s_or_b32 s4, s4, s40
	s_getpc_b64 s[38:39]
	v_lshlrev_b32_e32 v240, 7, v0
	v_min_u32_e32 v240, 0x3380, v240
	global_load_dword v241, v240, s[38:39]
	s_mov_b32 s5, 0
	s_mov_b32 s28, s3
	s_load_dwordx8 s[20:27], s[0:1], 0x0
	s_mov_b32 s3, s5
	s_lshl_b64 s[0:1], s[4:5], 12
	s_lshl_b64 s[2:3], s[2:3], 8
	s_add_u32 s0, s0, s2
	v_lshrrev_b32_e32 v1, 6, v0
	s_addc_u32 s1, s1, s3
	v_and_b32_e32 v160, 31, v0
	s_lshl_b64 s[2:3], s[0:1], 8
	v_lshlrev_b32_e32 v162, 5, v1
	s_waitcnt lgkmcnt(0)
	s_add_u32 s2, s20, s2
	v_or_b32_e32 v2, v162, v160
	v_bfe_u32 v54, v0, 5, 1
	s_addc_u32 s3, s21, s3
	v_and_b32_e32 v164, 63, v0
	v_lshrrev_b32_e32 v165, 4, v164
	v_add_u32_e32 v165, v162, v165
	v_lshlrev_b32_e32 v165, 8, v165
	v_and_b32_e32 v164, 15, v164
	v_lshl_add_u32 v164, v164, 4, v165
	v_mov_b32_e32 v165, 0
	v_lshl_add_u64 v[2:3], s[2:3], 0, v[164:165]
	s_mov_b64 s[6:7], 0x1000
	v_lshl_add_u64 v[4:5], v[2:3], 0, s[6:7]
	global_load_dwordx4 v[156:159], v[2:3], off
	global_load_dwordx4 v[152:155], v[2:3], off offset:1024
	global_load_dwordx4 v[148:151], v[2:3], off offset:2048
	global_load_dwordx4 v[144:147], v[2:3], off offset:3072
	global_load_dwordx4 v[140:143], v[4:5], off
	global_load_dwordx4 v[136:139], v[4:5], off offset:1024
	global_load_dwordx4 v[132:135], v[4:5], off offset:2048
	global_load_dwordx4 v[128:131], v[4:5], off offset:3072
	v_lshlrev_b32_e32 v164, 4, v54
	s_ashr_i32 s29, s28, 31
	v_bfe_u32 v55, v0, 2, 3
	s_lshl_b64 s[2:3], s[4:5], 20
	s_lshl_b64 s[20:21], s[28:29], 18
	v_lshl_or_b32 v2, v1, 3, v55
	s_add_u32 s4, s22, s2
	v_lshrrev_b32_e32 v3, 2, v2
	s_addc_u32 s7, s23, s3
	v_xor_b32_e32 v4, v3, v0
	s_add_u32 s6, s4, s20
	v_and_b32_e32 v5, 32, v0
	v_lshlrev_b32_e32 v4, 3, v4
	v_lshlrev_b32_e32 v1, 11, v1
	s_addc_u32 s7, s7, s21
	v_lshlrev_b32_e32 v164, 8, v2
	v_and_or_b32 v4, v4, 24, v5
	v_add_u32_e32 v173, 0, v1
	v_lshl_add_u64 v[2:3], s[6:7], 0, v[164:165]
	v_lshlrev_b32_e32 v164, 1, v4
	v_readfirstlane_b32 s4, v173
	v_add_u32_e32 v6, 0x400, v173
	v_lshl_add_u64 v[2:3], v[2:3], 0, v[164:165]
	s_mov_b64 s[6:7], 0x80
	s_mov_b32 m0, s4
	v_readfirstlane_b32 s4, v6
	v_add_u32_e32 v6, 0x4000, v173
	v_lshl_add_u64 v[4:5], v[2:3], 0, s[6:7]
	global_load_lds_dwordx4 v[2:3], off
	s_mov_b32 m0, s4
	s_mov_b64 s[6:7], 0x4000
	v_readfirstlane_b32 s4, v6
	global_load_lds_dwordx4 v[4:5], off
	v_lshl_add_u64 v[4:5], v[2:3], 0, s[6:7]
	s_mov_b32 m0, s4
	s_mov_b64 s[6:7], 0x4080
	global_load_lds_dwordx4 v[4:5], off
	v_add_u32_e32 v4, 0x4400, v173
	v_lshl_add_u64 v[2:3], v[2:3], 0, s[6:7]
	v_readfirstlane_b32 s4, v4
	s_mov_b32 m0, s4
	s_movk_i32 s4, 0x1c0
	global_load_lds_dwordx4 v[2:3], off
	v_lshlrev_b32_e32 v2, 8, v0
	v_and_b32_e32 v2, 0x1800, v2
	v_lshlrev_b32_e32 v3, 6, v0
	v_and_or_b32 v6, v3, s4, v2
	v_xor_b32_e32 v2, v54, v55
	v_lshlrev_b32_e32 v2, 4, v2
	v_and_or_b32 v175, v2, 48, v6
	v_and_b32_e32 v190, 63, v0
	v_lshrrev_b32_e32 v191, 4, v190
	v_and_b32_e32 v192, 15, v190
	v_xor_b32_e32 v193, v192, v191
	v_lshlrev_b32_e32 v193, 4, v193
	v_add_u32_e32 v194, v162, v191
	v_lshlrev_b32_e32 v194, 8, v194
	v_add_u32_e32 v194, 0x10000, v194
	v_and_b32_e32 v195, 15, v160
	v_xor_b32_e32 v195, v195, v54
	v_lshlrev_b32_e32 v195, 4, v195
	v_add_u32_e32 v196, v162, v160
	v_lshlrev_b32_e32 v196, 8, v196
	v_add_u32_e32 v196, 0x10000, v196
	s_waitcnt vmcnt(4)
	v_xor_b32_e32 v197, 0x0, v193
	v_add_u32_e32 v197, v197, v194
	ds_write_b128 v197, v[156:159] offset:0
	v_xor_b32_e32 v197, 0x40, v193
	v_add_u32_e32 v197, v197, v194
	ds_write_b128 v197, v[152:155] offset:1024
	v_xor_b32_e32 v197, 0x80, v193
	v_add_u32_e32 v197, v197, v194
	ds_write_b128 v197, v[148:151] offset:2048
	v_xor_b32_e32 v197, 0xc0, v193
	v_add_u32_e32 v197, v197, v194
	ds_write_b128 v197, v[144:147] offset:3072
	v_xor_b32_e32 v197, 0x0, v193
	v_add_u32_e32 v197, v197, v194
	ds_write_b128 v197, v[140:143] offset:4096
	v_xor_b32_e32 v197, 0x40, v193
	v_add_u32_e32 v197, v197, v194
	ds_write_b128 v197, v[136:139] offset:5120
	v_xor_b32_e32 v197, 0x80, v193
	v_add_u32_e32 v197, v197, v194
	ds_write_b128 v197, v[132:135] offset:6144
	v_xor_b32_e32 v197, 0xc0, v193
	v_add_u32_e32 v197, v197, v194
	ds_write_b128 v197, v[128:131] offset:7168
	s_waitcnt lgkmcnt(0)
	v_xor_b32_e32 v198, 0x0, v195
	v_add_u32_e32 v198, v198, v196
	ds_read_b128 v[156:159], v198
	v_xor_b32_e32 v198, 0x20, v195
	v_add_u32_e32 v198, v198, v196
	ds_read_b128 v[152:155], v198
	v_xor_b32_e32 v198, 0x40, v195
	v_add_u32_e32 v198, v198, v196
	ds_read_b128 v[148:151], v198
	v_xor_b32_e32 v198, 0x60, v195
	v_add_u32_e32 v198, v198, v196
	ds_read_b128 v[144:147], v198
	v_xor_b32_e32 v198, 0x80, v195
	v_add_u32_e32 v198, v198, v196
	ds_read_b128 v[140:143], v198
	v_xor_b32_e32 v198, 0xa0, v195
	v_add_u32_e32 v198, v198, v196
	ds_read_b128 v[136:139], v198
	v_xor_b32_e32 v198, 0xc0, v195
	v_add_u32_e32 v198, v198, v196
	ds_read_b128 v[132:135], v198
	v_xor_b32_e32 v198, 0xe0, v195
	v_add_u32_e32 v198, v198, v196
	ds_read_b128 v[128:131], v198
	s_waitcnt vmcnt(2)
	v_add_u32_e32 v172, 0, v175
	s_waitcnt lgkmcnt(0)
	s_barrier
	ds_read_b128 v[2:5], v172
	ds_read_b128 v[34:37], v172 offset:512
	v_bitop3_b32 v7, v54, v55, 2 bitop3:0x36
	v_lshlrev_b32_e32 v7, 4, v7
	v_and_or_b32 v176, v7, 48, v6
	v_add_u32_e32 v174, 0, v176
	ds_read_b128 v[18:21], v174
	ds_read_b128 v[38:41], v174 offset:512
	s_mov_b32 s33, 0x41200000
	s_cmp_lg_u32 0, -1
	s_cselect_b32 s37, 0, 0
	s_waitcnt vmcnt(2) lgkmcnt(0)
	v_mfma_f32_32x32x16_f16 v[2:17], v[2:5], v[156:159], 0
	s_movk_i32 s4, 0x110
	v_and_b32_e32 v161, 63, v0
	v_lshl_or_b32 v1, v55, 8, v1
	s_mov_b32 s18, s5
	s_mov_b32 s19, s5
	s_mov_b32 s6, s5
	s_mov_b32 s7, s5
	v_mfma_f32_32x32x16_f16 v[2:17], v[18:21], v[152:155], v[2:17]
	ds_read_b128 v[18:21], v172 offset:8192
	ds_read_b128 v[42:45], v172 offset:8704
	ds_read_b128 v[46:49], v174 offset:8192
	ds_read_b128 v[50:53], v174 offset:8704
	s_mov_b32 s8, s5
	s_mov_b32 s9, s5
	s_mov_b32 s10, s5
	s_mov_b32 s11, s5
	s_mov_b32 s12, s5
	s_waitcnt lgkmcnt(3)
	v_mfma_f32_32x32x16_f16 v[18:33], v[18:21], v[156:159], 0
	s_mov_b32 s13, s5
	s_mov_b32 s14, s5
	s_mov_b32 s15, s5
	s_mov_b32 s16, s5
	s_mov_b32 s17, s5
	s_mov_b32 s36, 1
	s_mov_b32 s34, -1
	s_waitcnt lgkmcnt(1)
	v_mfma_f32_32x32x16_f16 v[18:33], v[46:49], v[152:155], v[18:33]
	s_mov_b32 s35, 2
	s_mov_b64 s[30:31], 0x8000
	v_mfma_f32_32x32x16_f16 v[2:17], v[34:37], v[148:151], v[2:17]
	v_mfma_f32_32x32x16_f16 v[18:33], v[42:45], v[148:151], v[18:33]
	v_mfma_f32_32x32x16_f16 v[2:17], v[38:41], v[144:147], v[2:17]
	ds_read_b128 v[34:37], v172 offset:1024
	ds_read_b128 v[38:41], v172 offset:1536
	s_waitcnt lgkmcnt(2)
	v_mfma_f32_32x32x16_f16 v[18:33], v[50:53], v[144:147], v[18:33]
	s_waitcnt lgkmcnt(1)
	v_mfma_f32_32x32x16_f16 v[2:17], v[34:37], v[140:143], v[2:17]
	ds_read_b128 v[34:37], v172 offset:9216
	ds_read_b128 v[42:45], v172 offset:9728
	s_waitcnt lgkmcnt(1)
	v_mfma_f32_32x32x16_f16 v[18:33], v[34:37], v[140:143], v[18:33]
	ds_read_b128 v[34:37], v174 offset:1024
	ds_read_b128 v[46:49], v174 offset:1536
	s_waitcnt lgkmcnt(1)
	v_mfma_f32_32x32x16_f16 v[2:17], v[34:37], v[136:139], v[2:17]
	ds_read_b128 v[34:37], v174 offset:9216
	ds_read_b128 v[50:53], v174 offset:9728
	v_mfma_f32_32x32x16_f16 v[2:17], v[38:41], v[132:135], v[2:17]
	s_waitcnt lgkmcnt(1)
	v_mfma_f32_32x32x16_f16 v[18:33], v[34:37], v[136:139], v[18:33]
	v_mov_b32_e32 v34, 0xf149f2ca
	v_mfma_f32_32x32x16_f16 v[2:17], v[46:49], v[128:131], v[2:17]
	v_mfma_f32_32x32x16_f16 v[18:33], v[42:45], v[132:135], v[18:33]
	s_nop 10
	v_max_f32_e32 v35, v3, v3
	v_max_f32_e32 v36, v2, v2
	v_max_f32_e32 v35, v36, v35
	v_max3_f32 v35, v35, v4, v5
	v_max3_f32 v35, v35, v6, v7
	v_max3_f32 v35, v35, v8, v9
	v_max3_f32 v35, v35, v10, v11
	s_waitcnt lgkmcnt(0)
	v_mfma_f32_32x32x16_f16 v[18:33], v[50:53], v[128:131], v[18:33]
	v_max3_f32 v35, v35, v12, v13
	v_max3_f32 v35, v35, v14, v15
	v_max3_f32 v35, v35, v16, v17
	s_nop 8
	v_max3_f32 v35, v35, v18, v19
	v_max3_f32 v35, v35, v20, v21
	v_max3_f32 v35, v35, v22, v23
	v_max3_f32 v35, v35, v24, v25
	v_max3_f32 v35, v35, v26, v27
	v_max3_f32 v35, v35, v28, v29
	v_max3_f32 v35, v35, v30, v31
	v_max3_f32 v35, v35, v32, v33
	v_mov_b32_e32 v36, v35
	s_nop 1
	v_permlane32_swap_b32_e32 v35, v36
	v_max_f32_e32 v36, v36, v36
	v_max_f32_e32 v35, v35, v35
	v_max_f32_e32 v35, v35, v36
	v_add_f32_e32 v36, 0x7149f2ca, v35
	v_cmp_ge_f32_e32 vcc, s33, v36
	s_cmp_eq_u64 vcc, exec
	v_max_f32_e32 v35, 0xf149f2ca, v35
	s_cselect_b64 vcc, -1, 0
	v_cndmask_b32_e32 v168, v35, v34, vcc
	v_sub_f32_e32 v96, v18, v168
	v_sub_f32_e32 v97, v19, v168
	v_lshlrev_b32_e32 v18, 4, v0
	v_lshrrev_b32_e32 v19, 4, v0
	v_sub_f32_e32 v98, v20, v168
	v_and_b32_e32 v18, 0xc0, v18
	v_bitop3_b32 v19, v19, v54, 1 bitop3:0x6c
	v_lshlrev_b32_e32 v20, 3, v0
	v_sub_f32_e32 v99, v21, v168
	v_lshl_or_b32 v18, v54, 11, v18
	v_lshlrev_b32_e32 v19, 5, v19
	v_and_b32_e32 v21, 8, v20
	v_or3_b32 v18, v18, v21, v19
	v_and_b32_e32 v19, 16, v20
	v_sub_f32_e32 v0, 0xf149f2ca, v35
	v_add3_u32 v163, v19, s37, v18
	v_bitop3_b32 v169, v18, s4, v19 bitop3:0x36
	v_exp_f32_e32 v18, v0
	s_add_u32 s2, s2, s20
	v_sub_f32_e32 v2, v2, v168
	v_sub_f32_e32 v3, v3, v168
	v_sub_f32_e32 v4, v4, v168
	v_sub_f32_e32 v5, v5, v168
	v_sub_f32_e32 v6, v6, v168
	v_sub_f32_e32 v7, v7, v168
	v_sub_f32_e32 v8, v8, v168
	v_sub_f32_e32 v9, v9, v168
	v_sub_f32_e32 v10, v10, v168
	v_sub_f32_e32 v11, v11, v168
	v_sub_f32_e32 v12, v12, v168
	v_sub_f32_e32 v13, v13, v168
	v_sub_f32_e32 v14, v14, v168
	v_sub_f32_e32 v15, v15, v168
	v_sub_f32_e32 v16, v16, v168
	v_sub_f32_e32 v17, v17, v168
	s_addc_u32 s3, s3, s21
	s_mov_b32 s4, s5
	v_exp_f32_e32 v127, v2
	v_exp_f32_e32 v180, v3
	v_exp_f32_e32 v125, v4
	v_exp_f32_e32 v179, v5
	v_exp_f32_e32 v123, v6
	v_exp_f32_e32 v126, v7
	v_exp_f32_e32 v122, v8
	v_exp_f32_e32 v124, v9
	v_exp_f32_e32 v119, v10
	v_exp_f32_e32 v121, v11
	v_exp_f32_e32 v117, v12
	v_exp_f32_e32 v120, v13
	v_exp_f32_e32 v115, v14
	v_exp_f32_e32 v118, v15
	v_exp_f32_e32 v114, v16
	v_exp_f32_e32 v116, v17
	v_or3_b32 v0, s2, v1, v164
	v_mov_b32_e32 v1, s3
	v_lshlrev_b32_e32 v164, 3, v54
	v_mov_b64_e32 v[62:63], s[18:19]
	v_lshl_add_u64 v[0:1], s[22:23], 0, v[0:1]
	s_mov_b64 s[2:3], 0xc080
	v_mov_b64_e32 v[48:49], s[4:5]
	v_sub_f32_e32 v100, v22, v168
	v_sub_f32_e32 v101, v23, v168
	v_sub_f32_e32 v102, v24, v168
	v_sub_f32_e32 v103, v25, v168
	v_sub_f32_e32 v104, v26, v168
	v_sub_f32_e32 v105, v27, v168
	v_sub_f32_e32 v106, v28, v168
	v_sub_f32_e32 v107, v29, v168
	v_sub_f32_e32 v108, v30, v168
	v_sub_f32_e32 v109, v31, v168
	v_sub_f32_e32 v110, v32, v168
	v_sub_f32_e32 v111, v33, v168
	v_lshl_add_u64 v[170:171], v[0:1], 0, s[2:3]
	s_movk_i32 s2, 0xbf80
	s_movk_i32 s20, 0xc000
	s_movk_i32 s22, 0xff80
	v_mov_b32_e32 v166, 1.0
	v_mov_b64_e32 v[60:61], s[16:17]
	v_mov_b64_e32 v[58:59], s[14:15]
	v_mov_b64_e32 v[56:57], s[12:13]
	v_mov_b64_e32 v[54:55], s[10:11]
	v_mov_b64_e32 v[52:53], s[8:9]
	v_mov_b64_e32 v[50:51], s[6:7]
	v_mov_b64_e32 v[32:33], v[48:49]
	v_mov_b64_e32 v[16:17], v[48:49]
	v_mov_b64_e32 v[0:1], v[48:49]
	s_mov_b32 s3, -1
	s_mov_b32 s21, -1
	s_mov_b32 s23, -1
	v_add_u32_e32 v167, s37, v169
	v_mov_b64_e32 v[34:35], v[50:51]
	v_mov_b64_e32 v[36:37], v[52:53]
	v_mov_b64_e32 v[38:39], v[54:55]
	v_mov_b64_e32 v[40:41], v[56:57]
	v_mov_b64_e32 v[42:43], v[58:59]
	v_mov_b64_e32 v[44:45], v[60:61]
	v_mov_b64_e32 v[46:47], v[62:63]
	v_mov_b64_e32 v[18:19], v[50:51]
	v_mov_b64_e32 v[20:21], v[52:53]
	v_mov_b64_e32 v[22:23], v[54:55]
	v_mov_b64_e32 v[24:25], v[56:57]
	v_mov_b64_e32 v[26:27], v[58:59]
	v_mov_b64_e32 v[28:29], v[60:61]
	v_mov_b64_e32 v[30:31], v[62:63]
	v_mov_b64_e32 v[2:3], v[50:51]
	v_mov_b64_e32 v[4:5], v[52:53]
	v_mov_b64_e32 v[6:7], v[54:55]
	v_mov_b64_e32 v[8:9], v[56:57]
	v_mov_b64_e32 v[10:11], v[58:59]
	v_mov_b64_e32 v[12:13], v[60:61]
	v_mov_b64_e32 v[14:15], v[62:63]

	.amdhsa_kernel _Z11attn_kernelPKDF16_S0_PDF16_P15HIP_vector_typeIfLj2EE
		.amdhsa_group_segment_fixed_size 81920
		.amdhsa_private_segment_fixed_size 0
		.amdhsa_kernarg_size 32
		.amdhsa_user_sgpr_count 2
		.amdhsa_user_sgpr_dispatch_ptr 0
		.amdhsa_user_sgpr_queue_ptr 0
		.amdhsa_user_sgpr_kernarg_segment_ptr 1
		.amdhsa_user_sgpr_dispatch_id 0
		.amdhsa_user_sgpr_kernarg_preload_length 0
		.amdhsa_user_sgpr_kernarg_preload_offset 0
		.amdhsa_user_sgpr_private_segment_size 0
		.amdhsa_uses_dynamic_stack 0
		.amdhsa_enable_private_segment 0
		.amdhsa_system_sgpr_workgroup_id_x 1
		.amdhsa_system_sgpr_workgroup_id_y 1
		.amdhsa_system_sgpr_workgroup_id_z 1
		.amdhsa_system_sgpr_workgroup_info 0
		.amdhsa_system_vgpr_workitem_id 0
		.amdhsa_next_free_vgpr 244
		.amdhsa_next_free_sgpr 42
		.amdhsa_accum_offset 244
		.amdhsa_reserve_vcc 1
		.amdhsa_float_round_mode_32 0
		.amdhsa_float_round_mode_16_64 0
		.amdhsa_float_denorm_mode_32 3
		.amdhsa_float_denorm_mode_16_64 3
		.amdhsa_dx10_clamp 1
		.amdhsa_ieee_mode 1
		.amdhsa_fp16_overflow 0
		.amdhsa_tg_split 0
		.amdhsa_exception_fp_ieee_invalid_op 0
		.amdhsa_exception_fp_denorm_src 0
		.amdhsa_exception_fp_ieee_div_zero 0
		.amdhsa_exception_fp_ieee_overflow 0
		.amdhsa_exception_fp_ieee_underflow 0
		.amdhsa_exception_fp_ieee_inexact 0
		.amdhsa_exception_int_div_zero 0
	.end_amdhsa_kernel

amdhsa.kernels:
  - .agpr_count:     32
    .args:
      - .actual_access:  read_only
        .address_space:  global
        .offset:         0
        .size:           8
        .value_kind:     global_buffer
      - .actual_access:  read_only
        .address_space:  global
        .offset:         8
        .size:           8
        .value_kind:     global_buffer
      - .actual_access:  read_only
        .address_space:  global
        .offset:         16
        .size:           8
        .value_kind:     global_buffer
      - .actual_access:  read_only
        .address_space:  global
        .offset:         24
        .size:           8
        .value_kind:     global_buffer
      - .actual_access:  write_only
        .address_space:  global
        .offset:         32
        .size:           8
        .value_kind:     global_buffer
      - .actual_access:  write_only
        .address_space:  global
        .offset:         40
        .size:           8
        .value_kind:     global_buffer
      - .actual_access:  read_only
        .address_space:  global
        .offset:         48
        .size:           8
        .value_kind:     global_buffer
      - .actual_access:  write_only
        .address_space:  global
        .offset:         56
        .size:           8
        .value_kind:     global_buffer
    .group_segment_fixed_size: 34816
    .kernarg_segment_align: 8
    .kernarg_segment_size: 64
    .language:       OpenCL C
    .language_version:
      - 2
      - 0
    .max_flat_workgroup_size: 256
    .name:           _Z11prep_kernelPKfS0_S0_S0_PDF16_S1_S0_S1_
    .private_segment_fixed_size: 0
    .sgpr_count:     30
    .sgpr_spill_count: 0
    .symbol:         _Z11prep_kernelPKfS0_S0_S0_PDF16_S1_S0_S1_.kd
    .uniform_work_group_size: 1
    .uses_dynamic_stack: false
    .vgpr_count:     220
    .vgpr_spill_count: 0
    .wavefront_size: 64
  - .agpr_count:     0
    .args:
      - .actual_access:  read_only
        .address_space:  global
        .offset:         0
        .size:           8
        .value_kind:     global_buffer
      - .address_space:  global
        .offset:         8
        .size:           8
        .value_kind:     global_buffer
      - .actual_access:  write_only
        .address_space:  global
        .offset:         16
        .size:           8
        .value_kind:     global_buffer
      - .actual_access:  write_only
        .address_space:  global
        .offset:         24
        .size:           8
        .value_kind:     global_buffer
    .group_segment_fixed_size: 81920
    .kernarg_segment_align: 8
    .kernarg_segment_size: 32
    .language:       OpenCL C
    .language_version:
      - 2
      - 0
    .max_flat_workgroup_size: 512
    .name:           _Z11attn_kernelPKDF16_S0_PDF16_P15HIP_vector_typeIfLj2EE
    .private_segment_fixed_size: 0
    .sgpr_count:     48
    .sgpr_spill_count: 0
    .symbol:         _Z11attn_kernelPKDF16_S0_PDF16_P15HIP_vector_typeIfLj2EE.kd
    .uniform_work_group_size: 1
    .uses_dynamic_stack: false
    .vgpr_count:     244
    .vgpr_spill_count: 0
    .wavefront_size: 64
  - .agpr_count:     0
    .args:
      - .actual_access:  read_only
        .address_space:  global
        .offset:         0
        .size:           8
        .value_kind:     global_buffer
      - .actual_access:  read_only
        .address_space:  global
        .offset:         8
        .size:           8
        .value_kind:     global_buffer
      - .actual_access:  read_only
        .address_space:  global
        .offset:         16
        .size:           8
        .value_kind:     global_buffer
      - .actual_access:  read_only
        .address_space:  global
        .offset:         24
        .size:           8
        .value_kind:     global_buffer
      - .actual_access:  write_only
        .address_space:  global
        .offset:         32
        .size:           8
        .value_kind:     global_buffer
    .group_segment_fixed_size: 50176
    .kernarg_segment_align: 8
    .kernarg_segment_size: 40
    .language:       OpenCL C
    .language_version:
      - 2
      - 0
    .max_flat_workgroup_size: 256
    .name:           _Z19combine_proj_kernelPKDF16_PK15HIP_vector_typeIfLj2EES0_PKfPf
    .private_segment_fixed_size: 0
    .sgpr_count:     50
    .sgpr_spill_count: 0
    .symbol:         _Z19combine_proj_kernelPKDF16_PK15HIP_vector_typeIfLj2EES0_PKfPf.kd
    .uniform_work_group_size: 1
    .uses_dynamic_stack: false
    .vgpr_count:     220
    .vgpr_spill_count: 0
    .wavefront_size: 64
